# combine loop output stores marked nt (f32 output is written once and never re-read by the kernel)
# baseline (speedup 1.0000x reference)
.LBB0_2785:
	s_ashr_i32 s7, s6, 31
	s_lshl_b64 s[10:11], s[6:7], 2
	s_add_u32 s20, s14, s10
	s_addc_u32 s21, s15, s11
	global_load_dwordx2 v[10:11], v[4:5], off
	global_load_dwordx2 v[12:13], v1, s[20:21]
	s_add_i32 s22, s6, 1
	s_ashr_i32 s23, s22, 31
	s_add_u32 s10, s16, s10
	s_addc_u32 s11, s17, s11
	global_load_dword v0, v1, s[10:11]
	s_lshl_b64 s[20:21], s[22:23], 2
	s_add_u32 s10, s16, s20
	s_addc_u32 s11, s17, s21
	s_ashr_i32 s1, s0, 11
	s_mul_hi_i32 s3, s1, 0xc000
	s_mul_i32 s1, s1, 0xc000
	global_load_dword v8, v1, s[10:11]
	s_add_u32 s10, s12, s1
	s_addc_u32 s11, s13, s3
	global_load_dwordx4 v[18:21], v9, s[10:11]
	s_add_i32 s0, s0, s2
	s_add_i32 s6, s6, s18
	s_cmp_lt_i32 s0, 0x8000
	s_waitcnt vmcnt(4)
	v_lshlrev_b32_e32 v22, 16, v10
	v_and_b32_e32 v23, 0xffff0000, v10
	v_lshlrev_b32_e32 v24, 16, v11
	v_and_b32_e32 v25, 0xffff0000, v11
	s_waitcnt vmcnt(3)
	v_ashrrev_i32_e32 v11, 31, v12
	v_mov_b32_e32 v10, v12
	v_ashrrev_i32_e32 v27, 31, v13
	v_mov_b32_e32 v26, v13
	v_lshlrev_b64 v[10:11], 12, v[10:11]
	v_lshlrev_b64 v[12:13], 12, v[26:27]
	v_lshl_add_u64 v[10:11], v[2:3], 0, v[10:11]
	v_lshl_add_u64 v[12:13], v[2:3], 0, v[12:13]
	global_load_dwordx2 v[26:27], v[10:11], off
	global_load_dwordx2 v[28:29], v[12:13], off
	global_load_dwordx2 v[34:35], v[4:5], off offset:512
	global_load_dwordx2 v[36:37], v[10:11], off offset:512
	global_load_dwordx2 v[38:39], v[12:13], off offset:512
	global_load_dwordx4 v[40:43], v9, s[10:11] offset:1024
	global_load_dwordx2 v[44:45], v[4:5], off offset:1024
	global_load_dwordx2 v[46:47], v[10:11], off offset:1024
	global_load_dwordx2 v[48:49], v[12:13], off offset:1024
	global_load_dwordx4 v[50:53], v9, s[10:11] offset:2048
	global_load_dwordx2 v[54:55], v[4:5], off offset:1536
	global_load_dwordx2 v[56:57], v[10:11], off offset:1536
	global_load_dwordx2 v[58:59], v[12:13], off offset:1536
	global_load_dwordx4 v[60:63], v9, s[10:11] offset:3072
	global_load_dwordx2 v[64:65], v[4:5], off offset:2048
	global_load_dwordx2 v[66:67], v[10:11], off offset:2048
	global_load_dwordx2 v[68:69], v[12:13], off offset:2048
	global_load_dwordx4 v[70:73], v14, s[10:11]
	global_load_dwordx2 v[74:75], v[4:5], off offset:2560
	global_load_dwordx2 v[76:77], v[10:11], off offset:2560
	global_load_dwordx2 v[78:79], v[12:13], off offset:2560
	global_load_dwordx4 v[80:83], v15, s[10:11]
	global_load_dwordx2 v[84:85], v[4:5], off offset:3072
	global_load_dwordx2 v[86:87], v[10:11], off offset:3072
	global_load_dwordx2 v[88:89], v[12:13], off offset:3072
	global_load_dwordx4 v[90:93], v16, s[10:11]
	global_load_dwordx2 v[94:95], v[4:5], off offset:3584
	global_load_dwordx2 v[96:97], v[10:11], off offset:3584
	global_load_dwordx2 v[98:99], v[12:13], off offset:3584
	global_load_dwordx4 v[100:103], v17, s[10:11]
	s_waitcnt vmcnt(29)
	v_lshlrev_b32_e32 v30, 16, v26
	s_waitcnt vmcnt(28)
	v_lshlrev_b32_e32 v32, 16, v28
	v_and_b32_e32 v33, 0xffff0000, v28
	v_lshlrev_b32_e32 v28, 16, v29
	v_and_b32_e32 v29, 0xffff0000, v29
	v_and_b32_e32 v31, 0xffff0000, v26
	v_lshlrev_b32_e32 v26, 16, v27
	v_and_b32_e32 v27, 0xffff0000, v27
	v_pk_mul_f32 v[32:33], v[8:9], v[32:33] op_sel_hi:[0,1]
	v_pk_mul_f32 v[28:29], v[8:9], v[28:29] op_sel_hi:[0,1]
	v_pk_fma_f32 v[30:31], v[0:1], v[30:31], v[32:33] op_sel_hi:[0,1,1]
	v_pk_fma_f32 v[26:27], v[0:1], v[26:27], v[28:29] op_sel_hi:[0,1,1]
	v_pk_fma_f32 v[18:19], v[18:19], v[30:31], v[22:23]
	v_pk_fma_f32 v[20:21], v[20:21], v[26:27], v[24:25]
	global_store_dwordx4 v[6:7], v[18:21], off offset:-4096 nt
	s_nop 0
	s_nop 0
	s_nop 0
	s_nop 0
	s_nop 0
	s_waitcnt vmcnt(25)
	v_mov_b32_e32 v22, v34
	v_mov_b32_e32 v23, v35
	v_mov_b32_e32 v24, v36
	v_mov_b32_e32 v25, v37
	v_mov_b32_e32 v26, v38
	v_mov_b32_e32 v27, v39
	v_mov_b32_e32 v18, v40
	v_mov_b32_e32 v19, v41
	v_mov_b32_e32 v20, v42
	v_mov_b32_e32 v21, v43
	v_lshlrev_b32_e32 v28, 16, v22
	s_nop 0
	v_lshlrev_b32_e32 v30, 16, v24
	s_nop 0
	v_lshlrev_b32_e32 v32, 16, v26
	v_and_b32_e32 v33, 0xffff0000, v26
	v_lshlrev_b32_e32 v26, 16, v27
	v_and_b32_e32 v27, 0xffff0000, v27
	v_and_b32_e32 v31, 0xffff0000, v24
	v_lshlrev_b32_e32 v24, 16, v25
	v_and_b32_e32 v25, 0xffff0000, v25
	v_pk_mul_f32 v[32:33], v[8:9], v[32:33] op_sel_hi:[0,1]
	v_pk_mul_f32 v[26:27], v[8:9], v[26:27] op_sel_hi:[0,1]
	v_and_b32_e32 v29, 0xffff0000, v22
	v_lshlrev_b32_e32 v22, 16, v23
	v_and_b32_e32 v23, 0xffff0000, v23
	v_pk_fma_f32 v[30:31], v[0:1], v[30:31], v[32:33] op_sel_hi:[0,1,1]
	v_pk_fma_f32 v[24:25], v[0:1], v[24:25], v[26:27] op_sel_hi:[0,1,1]
	s_nop 0
	v_pk_fma_f32 v[18:19], v[18:19], v[30:31], v[28:29]
	v_pk_fma_f32 v[20:21], v[20:21], v[24:25], v[22:23]
	global_store_dwordx4 v[6:7], v[18:21], off offset:-3072 nt
	s_nop 0
	s_nop 0
	s_nop 0
	s_nop 0
	s_nop 0
	s_waitcnt vmcnt(22)
	v_mov_b32_e32 v22, v44
	v_mov_b32_e32 v23, v45
	v_mov_b32_e32 v24, v46
	v_mov_b32_e32 v25, v47
	v_mov_b32_e32 v26, v48
	v_mov_b32_e32 v27, v49
	v_mov_b32_e32 v18, v50
	v_mov_b32_e32 v19, v51
	v_mov_b32_e32 v20, v52
	v_mov_b32_e32 v21, v53
	v_lshlrev_b32_e32 v28, 16, v22
	s_nop 0
	v_lshlrev_b32_e32 v30, 16, v24
	s_nop 0
	v_lshlrev_b32_e32 v32, 16, v26
	v_and_b32_e32 v33, 0xffff0000, v26
	v_lshlrev_b32_e32 v26, 16, v27
	v_and_b32_e32 v27, 0xffff0000, v27
	v_and_b32_e32 v31, 0xffff0000, v24
	v_lshlrev_b32_e32 v24, 16, v25
	v_and_b32_e32 v25, 0xffff0000, v25
	v_pk_mul_f32 v[32:33], v[8:9], v[32:33] op_sel_hi:[0,1]
	v_pk_mul_f32 v[26:27], v[8:9], v[26:27] op_sel_hi:[0,1]
	v_and_b32_e32 v29, 0xffff0000, v22
	v_lshlrev_b32_e32 v22, 16, v23
	v_and_b32_e32 v23, 0xffff0000, v23
	v_pk_fma_f32 v[30:31], v[0:1], v[30:31], v[32:33] op_sel_hi:[0,1,1]
	v_pk_fma_f32 v[24:25], v[0:1], v[24:25], v[26:27] op_sel_hi:[0,1,1]
	s_nop 0
	v_pk_fma_f32 v[18:19], v[18:19], v[30:31], v[28:29]
	v_pk_fma_f32 v[20:21], v[20:21], v[24:25], v[22:23]
	global_store_dwordx4 v[6:7], v[18:21], off offset:-2048 nt
	s_nop 0
	s_nop 0
	s_nop 0
	s_nop 0
	s_nop 0
	s_waitcnt vmcnt(19)
	v_mov_b32_e32 v22, v54
	v_mov_b32_e32 v23, v55
	v_mov_b32_e32 v24, v56
	v_mov_b32_e32 v25, v57
	v_mov_b32_e32 v26, v58
	v_mov_b32_e32 v27, v59
	v_mov_b32_e32 v18, v60
	v_mov_b32_e32 v19, v61
	v_mov_b32_e32 v20, v62
	v_mov_b32_e32 v21, v63
	v_lshlrev_b32_e32 v28, 16, v22
	s_nop 0
	v_lshlrev_b32_e32 v30, 16, v24
	s_nop 0
	v_lshlrev_b32_e32 v32, 16, v26
	v_and_b32_e32 v33, 0xffff0000, v26
	v_lshlrev_b32_e32 v26, 16, v27
	v_and_b32_e32 v27, 0xffff0000, v27
	v_and_b32_e32 v31, 0xffff0000, v24
	v_lshlrev_b32_e32 v24, 16, v25
	v_and_b32_e32 v25, 0xffff0000, v25
	v_pk_mul_f32 v[32:33], v[8:9], v[32:33] op_sel_hi:[0,1]
	v_pk_mul_f32 v[26:27], v[8:9], v[26:27] op_sel_hi:[0,1]
	v_and_b32_e32 v29, 0xffff0000, v22
	v_lshlrev_b32_e32 v22, 16, v23
	v_and_b32_e32 v23, 0xffff0000, v23
	v_pk_fma_f32 v[30:31], v[0:1], v[30:31], v[32:33] op_sel_hi:[0,1,1]
	v_pk_fma_f32 v[24:25], v[0:1], v[24:25], v[26:27] op_sel_hi:[0,1,1]
	s_nop 0
	v_pk_fma_f32 v[18:19], v[18:19], v[30:31], v[28:29]
	v_pk_fma_f32 v[20:21], v[20:21], v[24:25], v[22:23]
	global_store_dwordx4 v[6:7], v[18:21], off offset:-1024 nt
	s_nop 0
	s_nop 0
	s_nop 0
	s_nop 0
	s_nop 0
	s_waitcnt vmcnt(16)
	v_mov_b32_e32 v22, v64
	v_mov_b32_e32 v23, v65
	v_mov_b32_e32 v24, v66
	v_mov_b32_e32 v25, v67
	v_mov_b32_e32 v26, v68
	v_mov_b32_e32 v27, v69
	v_mov_b32_e32 v18, v70
	v_mov_b32_e32 v19, v71
	v_mov_b32_e32 v20, v72
	v_mov_b32_e32 v21, v73
	v_lshlrev_b32_e32 v28, 16, v22
	s_nop 0
	v_lshlrev_b32_e32 v30, 16, v24
	s_nop 0
	v_lshlrev_b32_e32 v32, 16, v26
	v_and_b32_e32 v33, 0xffff0000, v26
	v_lshlrev_b32_e32 v26, 16, v27
	v_and_b32_e32 v27, 0xffff0000, v27
	v_and_b32_e32 v31, 0xffff0000, v24
	v_lshlrev_b32_e32 v24, 16, v25
	v_and_b32_e32 v25, 0xffff0000, v25
	v_pk_mul_f32 v[32:33], v[8:9], v[32:33] op_sel_hi:[0,1]
	v_pk_mul_f32 v[26:27], v[8:9], v[26:27] op_sel_hi:[0,1]
	v_and_b32_e32 v29, 0xffff0000, v22
	v_lshlrev_b32_e32 v22, 16, v23
	v_and_b32_e32 v23, 0xffff0000, v23
	v_pk_fma_f32 v[30:31], v[0:1], v[30:31], v[32:33] op_sel_hi:[0,1,1]
	v_pk_fma_f32 v[24:25], v[0:1], v[24:25], v[26:27] op_sel_hi:[0,1,1]
	s_nop 0
	v_pk_fma_f32 v[18:19], v[18:19], v[30:31], v[28:29]
	v_pk_fma_f32 v[20:21], v[20:21], v[24:25], v[22:23]
	global_store_dwordx4 v[6:7], v[18:21], off nt
	s_nop 0
	s_nop 0
	s_nop 0
	s_nop 0
	s_nop 0
	s_waitcnt vmcnt(13)
	v_mov_b32_e32 v22, v74
	v_mov_b32_e32 v23, v75
	v_mov_b32_e32 v24, v76
	v_mov_b32_e32 v25, v77
	v_mov_b32_e32 v26, v78
	v_mov_b32_e32 v27, v79
	v_mov_b32_e32 v18, v80
	v_mov_b32_e32 v19, v81
	v_mov_b32_e32 v20, v82
	v_mov_b32_e32 v21, v83
	v_lshlrev_b32_e32 v28, 16, v22
	s_nop 0
	v_lshlrev_b32_e32 v30, 16, v24
	s_nop 0
	v_lshlrev_b32_e32 v32, 16, v26
	v_and_b32_e32 v33, 0xffff0000, v26
	v_lshlrev_b32_e32 v26, 16, v27
	v_and_b32_e32 v27, 0xffff0000, v27
	v_and_b32_e32 v31, 0xffff0000, v24
	v_lshlrev_b32_e32 v24, 16, v25
	v_and_b32_e32 v25, 0xffff0000, v25
	v_pk_mul_f32 v[32:33], v[8:9], v[32:33] op_sel_hi:[0,1]
	v_pk_mul_f32 v[26:27], v[8:9], v[26:27] op_sel_hi:[0,1]
	v_and_b32_e32 v29, 0xffff0000, v22
	v_lshlrev_b32_e32 v22, 16, v23
	v_and_b32_e32 v23, 0xffff0000, v23
	v_pk_fma_f32 v[30:31], v[0:1], v[30:31], v[32:33] op_sel_hi:[0,1,1]
	v_pk_fma_f32 v[24:25], v[0:1], v[24:25], v[26:27] op_sel_hi:[0,1,1]
	s_nop 0
	v_pk_fma_f32 v[18:19], v[18:19], v[30:31], v[28:29]
	v_pk_fma_f32 v[20:21], v[20:21], v[24:25], v[22:23]
	global_store_dwordx4 v[6:7], v[18:21], off offset:1024 nt
	s_nop 0
	s_nop 0
	s_nop 0
	s_nop 0
	s_nop 0
	s_waitcnt vmcnt(10)
	v_mov_b32_e32 v22, v84
	v_mov_b32_e32 v23, v85
	v_mov_b32_e32 v24, v86
	v_mov_b32_e32 v25, v87
	v_mov_b32_e32 v26, v88
	v_mov_b32_e32 v27, v89
	v_mov_b32_e32 v18, v90
	v_mov_b32_e32 v19, v91
	v_mov_b32_e32 v20, v92
	v_mov_b32_e32 v21, v93
	v_lshlrev_b32_e32 v28, 16, v22
	s_nop 0
	v_lshlrev_b32_e32 v30, 16, v24
	s_nop 0
	v_lshlrev_b32_e32 v32, 16, v26
	v_and_b32_e32 v33, 0xffff0000, v26
	v_lshlrev_b32_e32 v26, 16, v27
	v_and_b32_e32 v27, 0xffff0000, v27
	v_and_b32_e32 v31, 0xffff0000, v24
	v_lshlrev_b32_e32 v24, 16, v25
	v_and_b32_e32 v25, 0xffff0000, v25
	v_pk_mul_f32 v[32:33], v[8:9], v[32:33] op_sel_hi:[0,1]
	v_pk_mul_f32 v[26:27], v[8:9], v[26:27] op_sel_hi:[0,1]
	v_and_b32_e32 v29, 0xffff0000, v22
	v_lshlrev_b32_e32 v22, 16, v23
	v_and_b32_e32 v23, 0xffff0000, v23
	v_pk_fma_f32 v[30:31], v[0:1], v[30:31], v[32:33] op_sel_hi:[0,1,1]
	v_pk_fma_f32 v[24:25], v[0:1], v[24:25], v[26:27] op_sel_hi:[0,1,1]
	s_nop 0
	v_pk_fma_f32 v[18:19], v[18:19], v[30:31], v[28:29]
	v_pk_fma_f32 v[20:21], v[20:21], v[24:25], v[22:23]
	global_store_dwordx4 v[6:7], v[18:21], off offset:2048 nt
	s_nop 0
	s_nop 0
	s_nop 0
	s_nop 0
	s_nop 0
	v_lshl_add_u64 v[4:5], v[4:5], 0, s[4:5]
	s_waitcnt vmcnt(7)
	v_mov_b32_e32 v22, v94
	v_mov_b32_e32 v23, v95
	v_mov_b32_e32 v24, v96
	v_mov_b32_e32 v25, v97
	v_mov_b32_e32 v26, v98
	v_mov_b32_e32 v27, v99
	v_mov_b32_e32 v18, v100
	v_mov_b32_e32 v19, v101
	v_mov_b32_e32 v20, v102
	v_mov_b32_e32 v21, v103
	v_lshlrev_b32_e32 v10, 16, v22
	s_nop 0
	v_lshlrev_b32_e32 v12, 16, v24
	s_nop 0
	v_lshlrev_b32_e32 v28, 16, v26
	v_and_b32_e32 v29, 0xffff0000, v26
	v_lshlrev_b32_e32 v26, 16, v27
	v_and_b32_e32 v27, 0xffff0000, v27
	v_and_b32_e32 v13, 0xffff0000, v24
	v_lshlrev_b32_e32 v24, 16, v25
	v_and_b32_e32 v25, 0xffff0000, v25
	v_pk_mul_f32 v[28:29], v[8:9], v[28:29] op_sel_hi:[0,1]
	v_pk_mul_f32 v[26:27], v[8:9], v[26:27] op_sel_hi:[0,1]
	v_and_b32_e32 v11, 0xffff0000, v22
	v_lshlrev_b32_e32 v22, 16, v23
	v_and_b32_e32 v23, 0xffff0000, v23
	v_pk_fma_f32 v[12:13], v[0:1], v[12:13], v[28:29] op_sel_hi:[0,1,1]
	v_pk_fma_f32 v[24:25], v[0:1], v[24:25], v[26:27] op_sel_hi:[0,1,1]
	s_nop 0
	v_pk_fma_f32 v[10:11], v[18:19], v[12:13], v[10:11]
	v_pk_fma_f32 v[12:13], v[20:21], v[24:25], v[22:23]
	global_store_dwordx4 v[6:7], v[10:13], off offset:3072 nt
	v_lshl_add_u64 v[6:7], v[6:7], 0, s[8:9]
	s_cbranch_scc1 .LBB0_2785
